# fp8 MoE GEMM K-loops: mid-segment priority flip pair (setprio 0 then 1 between the two 8-MFMA groups) removed, priority held at 1 across the 16 MFMAs
# baseline (speedup 1.0000x reference)
; #define PG8_STAGE(bufoff, gbase, voff) do { _Pragma("unroll") for (int _i = 0; _i < 2; ++_i) \
;         __builtin_amdgcn_global_load_lds((const unsigned*)((const char*)(gbase) + (voff)[_i]), (PG8_LAS unsigned*)(lds + (bufoff) + ldsw + _i * 8192), 16, 0, 0); } while (0)
; #define PG8_WAIT_V(n) asm volatile("s_waitcnt vmcnt(" #n ")" ::: "memory")
; #define PG8_WAIT_L(n) asm volatile("s_waitcnt lgkmcnt(" #n ")" ::: "memory")
; #define PG8_BAR __builtin_amdgcn_s_barrier()
; #define PG8_SCHED __builtin_amdgcn_sched_barrier(0)
; template <class Epi, class Sched, bool ALIGN_EPI = false, bool SP2 = false, bool FP8 = false, bool I8 = false>
; __device__ __forceinline__ void gemm_phase(PG8_LAS unsigned char* lds, const Gemm g, const Sched& S, const Epi& E) {
;     ...
;             PG8_LDA(At, 0, 1); PG8_STAGE(PG8_SB(0, 0), b2, voffB); PG8_STAGE(PG8_SB(0, 1), b2 + hstep, voffB); PG8_STAGE(PG8_SA(0, 0), a2, voffA);
;             PG8_WAIT_V(8); PG8_WAIT_L(0); PG8_BAR; PG8_MMA(1, 0, At, B0); PG8_MMA(1, 1, At, B1); PG8_BAR; PG8_SCHED;
;             PG8_LDB(B0, 1, 0); PG8_LDB(B1, 1, 1); PG8_SCHED; PG8_LDA(At, 1, 0); PG8_STAGE(PG8_SA(0, 1), a2 + hstepA, voffA1);
;             PG8_WAIT_V(8); PG8_WAIT_L(0); PG8_BAR; PG8_MMA(0, 0, At, B0); PG8_MMA(0, 1, At, B1); PG8_BAR; PG8_SCHED;
.LBB0_1917:
	v_lshl_add_u64 v[182:183], v[180:181], 0, s[2:3]
	s_add_u32 s61, s90, s2
	v_cndmask_b32_e64 v183, v183, v179, s[10:11]
	v_cndmask_b32_e64 v182, v182, v178, s[10:11]
	s_mov_b32 m0, s45
	s_addc_u32 s62, s91, s3
	v_lshl_add_u64 v[186:187], v[182:183], 0, v[166:167]
	s_add_u32 s61, s61, 0x34200100
	ds_read_b128 v[202:205], v198 offset:16384
	ds_read_b128 v[206:209], v198 offset:17408
	ds_read_b128 v[210:213], v198 offset:18432
	ds_read_b128 v[214:217], v198 offset:19456
	ds_read_b128 v[218:221], v198 offset:20480
	ds_read_b128 v[222:225], v198 offset:21504
	ds_read_b128 v[226:229], v198 offset:22528
	ds_read_b128 v[230:233], v198 offset:23552
	global_load_lds_dwordx4 v[186:187], off
	v_lshl_add_u64 v[184:185], v[182:183], 0, v[168:169]
	s_mov_b32 m0, s46
	v_lshl_add_u64 v[188:189], v[182:183], 0, s[18:19]
	s_addc_u32 s62, s62, 0
	global_load_lds_dwordx4 v[184:185], off
	v_lshl_add_u64 v[190:191], v[188:189], 0, v[166:167]
	s_mov_b32 m0, s47
	s_and_b64 s[10:11], s[10:11], exec
	global_load_lds_dwordx4 v[190:191], off
	v_lshl_add_u64 v[188:189], v[188:189], 0, v[168:169]
	s_mov_b32 m0, s48
	s_cselect_b32 s11, s15, s62
	s_cselect_b32 s10, s14, s61
	global_load_lds_dwordx4 v[188:189], off
	s_mov_b32 m0, s1
	v_mov_b32_e32 v173, v171
	global_load_lds_dwordx4 v172, s[10:11]
	s_mov_b32 m0, s49
	v_mov_b32_e32 v175, v171
	global_load_lds_dwordx4 v174, s[10:11]
	s_waitcnt vmcnt(8)
	s_waitcnt lgkmcnt(0)
	v_lshl_add_u64 v[190:191], s[10:11], 0, v[172:173]
	v_lshl_add_u64 v[188:189], s[10:11], 0, v[174:175]
	s_barrier
	s_setprio 1
	s_waitcnt lgkmcnt(0)
	v_mfma_scale_f32_16x16x128_f8f6f4 v[94:97], v[18:25], v[202:209], v[94:97], v197, v197 op_sel_hi:[0,0,0]
	v_mfma_scale_f32_16x16x128_f8f6f4 v[90:93], v[26:33], v[202:209], v[90:93], v197, v197 op_sel_hi:[0,0,0]
	v_mfma_scale_f32_16x16x128_f8f6f4 v[86:89], v[18:25], v[210:217], v[86:89], v197, v197 op_sel_hi:[0,0,0]
	v_mfma_scale_f32_16x16x128_f8f6f4 v[82:85], v[26:33], v[210:217], v[82:85], v197, v197 op_sel_hi:[0,0,0]
	v_mfma_scale_f32_16x16x128_f8f6f4 v[78:81], v[18:25], v[218:225], v[78:81], v197, v197 op_sel_hi:[0,0,0]
	v_mfma_scale_f32_16x16x128_f8f6f4 v[74:77], v[26:33], v[218:225], v[74:77], v197, v197 op_sel_hi:[0,0,0]
	v_mfma_scale_f32_16x16x128_f8f6f4 v[70:73], v[18:25], v[226:233], v[70:73], v197, v197 op_sel_hi:[0,0,0]
	v_mfma_scale_f32_16x16x128_f8f6f4 v[66:69], v[26:33], v[226:233], v[66:69], v197, v197 op_sel_hi:[0,0,0]
	v_mfma_scale_f32_16x16x128_f8f6f4 v[62:65], v[2:9], v[202:209], v[62:65], v197, v197 op_sel_hi:[0,0,0]
	v_mfma_scale_f32_16x16x128_f8f6f4 v[58:61], v[10:17], v[202:209], v[58:61], v197, v197 op_sel_hi:[0,0,0]
	v_mfma_scale_f32_16x16x128_f8f6f4 v[54:57], v[2:9], v[210:217], v[54:57], v197, v197 op_sel_hi:[0,0,0]
	v_mfma_scale_f32_16x16x128_f8f6f4 v[50:53], v[10:17], v[210:217], v[50:53], v197, v197 op_sel_hi:[0,0,0]
	v_mfma_scale_f32_16x16x128_f8f6f4 v[46:49], v[2:9], v[218:225], v[46:49], v197, v197 op_sel_hi:[0,0,0]
	v_mfma_scale_f32_16x16x128_f8f6f4 v[42:45], v[10:17], v[218:225], v[42:45], v197, v197 op_sel_hi:[0,0,0]
	v_mfma_scale_f32_16x16x128_f8f6f4 v[38:41], v[2:9], v[226:233], v[38:41], v197, v197 op_sel_hi:[0,0,0]
	v_mfma_scale_f32_16x16x128_f8f6f4 v[34:37], v[10:17], v[226:233], v[34:37], v197, v197 op_sel_hi:[0,0,0]
	s_setprio 0
	s_barrier
	s_add_i32 s61, 0, 0x18000
	s_add_i32 s62, 0, 0x1c000
	v_add_u32_e32 v14, s61, v195
	v_add_u32_e32 v30, s62, v195
	ds_read_b128 v[2:5], v14
	ds_read_b128 v[6:9], v14 offset:1024
	ds_read_b128 v[10:13], v14 offset:2048
	ds_read_b128 v[14:17], v14 offset:3072
	ds_read_b128 v[18:21], v30
	ds_read_b128 v[22:25], v30 offset:1024
	ds_read_b128 v[26:29], v30 offset:2048
	ds_read_b128 v[30:33], v30 offset:3072
	s_mov_b32 m0, s50
	v_lshl_add_u64 v[234:235], s[10:11], 0, v[170:171]
	ds_read_b128 v[202:205], v198 offset:32768
	ds_read_b128 v[206:209], v198 offset:33792
	ds_read_b128 v[210:213], v198 offset:34816
	ds_read_b128 v[214:217], v198 offset:35840
	ds_read_b128 v[218:221], v198 offset:36864
	ds_read_b128 v[222:225], v198 offset:37888
	ds_read_b128 v[226:229], v198 offset:38912
	ds_read_b128 v[230:233], v198 offset:39936
	global_load_lds_dwordx4 v[234:235], off
	v_lshl_add_u64 v[234:235], s[10:11], 0, v[176:177]
	s_mov_b32 m0, s51
	s_nop 0
	global_load_lds_dwordx4 v[234:235], off
	s_waitcnt vmcnt(8)
	s_waitcnt lgkmcnt(0)
	s_barrier
	s_setprio 1
	s_waitcnt lgkmcnt(0)
	v_mfma_scale_f32_16x16x128_f8f6f4 v[158:161], v[2:9], v[202:209], v[158:161], v197, v197 op_sel_hi:[0,0,0]
	v_mfma_scale_f32_16x16x128_f8f6f4 v[154:157], v[10:17], v[202:209], v[154:157], v197, v197 op_sel_hi:[0,0,0]
	v_mfma_scale_f32_16x16x128_f8f6f4 v[150:153], v[2:9], v[210:217], v[150:153], v197, v197 op_sel_hi:[0,0,0]
	v_mfma_scale_f32_16x16x128_f8f6f4 v[146:149], v[10:17], v[210:217], v[146:149], v197, v197 op_sel_hi:[0,0,0]
	v_mfma_scale_f32_16x16x128_f8f6f4 v[142:145], v[2:9], v[218:225], v[142:145], v197, v197 op_sel_hi:[0,0,0]
	v_mfma_scale_f32_16x16x128_f8f6f4 v[138:141], v[10:17], v[218:225], v[138:141], v197, v197 op_sel_hi:[0,0,0]
	v_mfma_scale_f32_16x16x128_f8f6f4 v[134:137], v[2:9], v[226:233], v[134:137], v197, v197 op_sel_hi:[0,0,0]
	v_mfma_scale_f32_16x16x128_f8f6f4 v[130:133], v[10:17], v[226:233], v[130:133], v197, v197 op_sel_hi:[0,0,0]
	v_mfma_scale_f32_16x16x128_f8f6f4 v[126:129], v[18:25], v[202:209], v[126:129], v197, v197 op_sel_hi:[0,0,0]
	v_mfma_scale_f32_16x16x128_f8f6f4 v[122:125], v[26:33], v[202:209], v[122:125], v197, v197 op_sel_hi:[0,0,0]
	v_mfma_scale_f32_16x16x128_f8f6f4 v[118:121], v[18:25], v[210:217], v[118:121], v197, v197 op_sel_hi:[0,0,0]
	v_mfma_scale_f32_16x16x128_f8f6f4 v[114:117], v[26:33], v[210:217], v[114:117], v197, v197 op_sel_hi:[0,0,0]
	v_mfma_scale_f32_16x16x128_f8f6f4 v[110:113], v[18:25], v[218:225], v[110:113], v197, v197 op_sel_hi:[0,0,0]
	v_mfma_scale_f32_16x16x128_f8f6f4 v[106:109], v[26:33], v[218:225], v[106:109], v197, v197 op_sel_hi:[0,0,0]
	v_mfma_scale_f32_16x16x128_f8f6f4 v[102:105], v[18:25], v[226:233], v[102:105], v197, v197 op_sel_hi:[0,0,0]
	v_mfma_scale_f32_16x16x128_f8f6f4 v[98:101], v[26:33], v[226:233], v[98:101], v197, v197 op_sel_hi:[0,0,0]
	s_setprio 0
	s_barrier
; #define PG8_ROWS(_u) do { _Pragma("unroll") for (int _i = 0; _i < 2; ++_i) { voffA[_i] = S.row_off((_u), rselA[_i]) + cselA[_i]; voffA1[_i] = S.row_off((_u), HALF + rselA[_i]) + cselA[_i]; } } while (0)
; #define PG8_STAGE(bufoff, gbase, voff) do { _Pragma("unroll") for (int _i = 0; _i < 2; ++_i) \
;         __builtin_amdgcn_global_load_lds((const unsigned*)((const char*)(gbase) + (voff)[_i]), (PG8_LAS unsigned*)(lds + (bufoff) + ldsw + _i * 8192), 16, 0, 0); } while (0)
; #define PG8_WAIT_V(n) asm volatile("s_waitcnt vmcnt(" #n ")" ::: "memory")
; #define PG8_WAIT_L(n) asm volatile("s_waitcnt lgkmcnt(" #n ")" ::: "memory")
; #define PG8_BAR __builtin_amdgcn_s_barrier()
; #define PG8_SCHED __builtin_amdgcn_sched_barrier(0)
; template <class Epi, class Sched, bool ALIGN_EPI = false, bool SP2 = false, bool FP8 = false, bool I8 = false>
; __device__ __forceinline__ void gemm_phase(PG8_LAS unsigned char* lds, const Gemm g, const Sched& S, const Epi& E) {
;     ...
;             PG8_LDB(B0, 0, 0); PG8_LDB(B1, 0, 1); PG8_SCHED; PG8_LDA(At, 0, 0); PG8_STAGE(PG8_SA(1, 1), a1 + hstepA, voffA1);
;             PG8_WAIT_V(8); PG8_WAIT_L(0); PG8_BAR; PG8_MMA(0, 0, At, B0); PG8_MMA(0, 1, At, B1); PG8_BAR; PG8_SCHED;
;             if constexpr (Sched::GATHER) { if (last && has_next) PG8_ROWS(ui + 1); }
;     ...
;             PG8_LDA(At, 1, 1); PG8_STAGE(PG8_SB(1, 0), b3, voffB); PG8_STAGE(PG8_SB(1, 1), b3 + hstep, voffB); PG8_STAGE(PG8_SA(1, 0), a3, voffA);
;             PG8_WAIT_V(8); PG8_WAIT_L(0); PG8_BAR; PG8_MMA(1, 0, At, B0); PG8_MMA(1, 1, At, B1); PG8_BAR; PG8_SCHED;
	s_add_i32 s10, s61, s44
	v_lshl_add_u64 v[186:187], v[186:187], 0, s[24:25]
	s_mov_b32 m0, s10
	ds_read_b128 v[202:205], v198 offset:49152
	ds_read_b128 v[206:209], v198 offset:50176
	ds_read_b128 v[210:213], v198 offset:51200
	ds_read_b128 v[214:217], v198 offset:52224
	ds_read_b128 v[218:221], v198 offset:53248
	ds_read_b128 v[222:225], v198 offset:54272
	ds_read_b128 v[226:229], v198 offset:55296
	ds_read_b128 v[230:233], v198 offset:56320
	global_load_lds_dwordx4 v[186:187], off
	v_lshl_add_u64 v[184:185], v[184:185], 0, s[24:25]
	s_add_i32 m0, s10, 0x2000
	v_lshl_add_u64 v[182:183], v[182:183], 0, s[28:29]
	s_add_i32 s10, s62, s44
	global_load_lds_dwordx4 v[184:185], off
	v_lshl_add_u64 v[184:185], v[182:183], 0, v[166:167]
	s_mov_b32 m0, s10
	v_lshl_add_u64 v[182:183], v[182:183], 0, v[168:169]
	global_load_lds_dwordx4 v[184:185], off
	s_add_i32 m0, s10, 0x2000
	s_nop 0
	global_load_lds_dwordx4 v[182:183], off
	v_lshl_add_u64 v[182:183], v[190:191], 0, s[24:25]
	s_mov_b32 m0, s53
	s_nop 0
	global_load_lds_dwordx4 v[182:183], off
	v_lshl_add_u64 v[182:183], v[188:189], 0, s[24:25]
	s_mov_b32 m0, s54
	s_nop 0
	global_load_lds_dwordx4 v[182:183], off
	s_waitcnt vmcnt(8)
	s_waitcnt lgkmcnt(0)
	s_barrier
	s_setprio 1
	s_waitcnt lgkmcnt(0)
	v_mfma_scale_f32_16x16x128_f8f6f4 v[94:97], v[2:9], v[202:209], v[94:97], v197, v197 op_sel_hi:[0,0,0]
	v_mfma_scale_f32_16x16x128_f8f6f4 v[90:93], v[10:17], v[202:209], v[90:93], v197, v197 op_sel_hi:[0,0,0]
	v_mfma_scale_f32_16x16x128_f8f6f4 v[86:89], v[2:9], v[210:217], v[86:89], v197, v197 op_sel_hi:[0,0,0]
	v_mfma_scale_f32_16x16x128_f8f6f4 v[82:85], v[10:17], v[210:217], v[82:85], v197, v197 op_sel_hi:[0,0,0]
	v_mfma_scale_f32_16x16x128_f8f6f4 v[78:81], v[2:9], v[218:225], v[78:81], v197, v197 op_sel_hi:[0,0,0]
	v_mfma_scale_f32_16x16x128_f8f6f4 v[74:77], v[10:17], v[218:225], v[74:77], v197, v197 op_sel_hi:[0,0,0]
	v_mfma_scale_f32_16x16x128_f8f6f4 v[70:73], v[2:9], v[226:233], v[70:73], v197, v197 op_sel_hi:[0,0,0]
	v_mfma_scale_f32_16x16x128_f8f6f4 v[66:69], v[10:17], v[226:233], v[66:69], v197, v197 op_sel_hi:[0,0,0]
	v_mfma_scale_f32_16x16x128_f8f6f4 v[62:65], v[18:25], v[202:209], v[62:65], v197, v197 op_sel_hi:[0,0,0]
	v_mfma_scale_f32_16x16x128_f8f6f4 v[58:61], v[26:33], v[202:209], v[58:61], v197, v197 op_sel_hi:[0,0,0]
	v_mfma_scale_f32_16x16x128_f8f6f4 v[54:57], v[18:25], v[210:217], v[54:57], v197, v197 op_sel_hi:[0,0,0]
	v_mfma_scale_f32_16x16x128_f8f6f4 v[50:53], v[26:33], v[210:217], v[50:53], v197, v197 op_sel_hi:[0,0,0]
	v_mfma_scale_f32_16x16x128_f8f6f4 v[46:49], v[18:25], v[218:225], v[46:49], v197, v197 op_sel_hi:[0,0,0]
	v_mfma_scale_f32_16x16x128_f8f6f4 v[42:45], v[26:33], v[218:225], v[42:45], v197, v197 op_sel_hi:[0,0,0]
	v_mfma_scale_f32_16x16x128_f8f6f4 v[38:41], v[18:25], v[226:233], v[38:41], v197, v197 op_sel_hi:[0,0,0]
	v_mfma_scale_f32_16x16x128_f8f6f4 v[34:37], v[26:33], v[226:233], v[34:37], v197, v197 op_sel_hi:[0,0,0]
	s_setprio 0
	s_barrier
	s_add_i32 s41, s41, 2
	s_add_u32 s2, s2, 0x100
	s_addc_u32 s3, s3, 0
	s_cmp_gt_u32 s41, 13
	s_cbranch_scc1 .LBB0_1920
.LBB0_1918:
	v_add_u32_e32 v2, 0, v195
	v_add_u32_e32 v3, 0x10000, v2
	v_add_u32_e32 v14, 0x14000, v2
	ds_read_b128 v[18:21], v3
	ds_read_b128 v[22:25], v3 offset:1024
	ds_read_b128 v[26:29], v3 offset:2048
	ds_read_b128 v[30:33], v3 offset:3072
	ds_read_b128 v[2:5], v14
	ds_read_b128 v[6:9], v14 offset:1024
	ds_read_b128 v[10:13], v14 offset:2048
	ds_read_b128 v[14:17], v14 offset:3072
	s_cmp_eq_u32 s41, 12
	s_cselect_b64 s[10:11], -1, 0
	s_add_u32 s62, s90, s2
	s_addc_u32 s63, s91, s3
	v_lshl_add_u64 v[190:191], s[62:63], 0, v[170:171]
	v_lshl_add_u64 v[190:191], v[190:191], 0, s[26:27]
	s_add_i32 m0, s1, 0xc000
	v_mov_b32_e32 v177, v171
	ds_read_b128 v[182:185], v198
	ds_read_b128 v[186:189], v198 offset:1024
	ds_read_b128 v[202:205], v198 offset:2048
	ds_read_b128 v[206:209], v198 offset:3072
	ds_read_b128 v[210:213], v198 offset:4096
	ds_read_b128 v[214:217], v198 offset:5120
	ds_read_b128 v[218:221], v198 offset:6144
	ds_read_b128 v[222:225], v198 offset:7168
	global_load_lds_dwordx4 v[190:191], off
	v_lshl_add_u64 v[190:191], s[62:63], 0, v[176:177]
	v_lshl_add_u64 v[190:191], v[190:191], 0, s[26:27]
	s_add_i32 m0, s1, 0xe000
	s_nop 0
	global_load_lds_dwordx4 v[190:191], off
	s_waitcnt vmcnt(8)
	s_waitcnt lgkmcnt(0)
	s_barrier
	s_setprio 1
	s_waitcnt lgkmcnt(0)
	v_mfma_scale_f32_16x16x128_f8f6f4 v[158:161], v[18:25], v[182:189], v[158:161], v197, v197 op_sel_hi:[0,0,0]
	v_mfma_scale_f32_16x16x128_f8f6f4 v[154:157], v[26:33], v[182:189], v[154:157], v197, v197 op_sel_hi:[0,0,0]
	v_mfma_scale_f32_16x16x128_f8f6f4 v[150:153], v[18:25], v[202:209], v[150:153], v197, v197 op_sel_hi:[0,0,0]
	v_mfma_scale_f32_16x16x128_f8f6f4 v[146:149], v[26:33], v[202:209], v[146:149], v197, v197 op_sel_hi:[0,0,0]
	v_mfma_scale_f32_16x16x128_f8f6f4 v[142:145], v[18:25], v[210:217], v[142:145], v197, v197 op_sel_hi:[0,0,0]
	v_mfma_scale_f32_16x16x128_f8f6f4 v[138:141], v[26:33], v[210:217], v[138:141], v197, v197 op_sel_hi:[0,0,0]
	v_mfma_scale_f32_16x16x128_f8f6f4 v[134:137], v[18:25], v[218:225], v[134:137], v197, v197 op_sel_hi:[0,0,0]
	v_mfma_scale_f32_16x16x128_f8f6f4 v[130:133], v[26:33], v[218:225], v[130:133], v197, v197 op_sel_hi:[0,0,0]
	v_mfma_scale_f32_16x16x128_f8f6f4 v[126:129], v[2:9], v[182:189], v[126:129], v197, v197 op_sel_hi:[0,0,0]
	v_mfma_scale_f32_16x16x128_f8f6f4 v[122:125], v[10:17], v[182:189], v[122:125], v197, v197 op_sel_hi:[0,0,0]
	v_mfma_scale_f32_16x16x128_f8f6f4 v[118:121], v[2:9], v[202:209], v[118:121], v197, v197 op_sel_hi:[0,0,0]
	v_mfma_scale_f32_16x16x128_f8f6f4 v[114:117], v[10:17], v[202:209], v[114:117], v197, v197 op_sel_hi:[0,0,0]
	v_mfma_scale_f32_16x16x128_f8f6f4 v[110:113], v[2:9], v[210:217], v[110:113], v197, v197 op_sel_hi:[0,0,0]
	v_mfma_scale_f32_16x16x128_f8f6f4 v[106:109], v[10:17], v[210:217], v[106:109], v197, v197 op_sel_hi:[0,0,0]
	v_mfma_scale_f32_16x16x128_f8f6f4 v[102:105], v[2:9], v[218:225], v[102:105], v197, v197 op_sel_hi:[0,0,0]
	v_mfma_scale_f32_16x16x128_f8f6f4 v[98:101], v[10:17], v[218:225], v[98:101], v197, v197 op_sel_hi:[0,0,0]
	s_and_b64 s[62:63], s[8:9], s[10:11]
	s_setprio 0
	s_barrier
	s_andn2_b64 vcc, exec, s[62:63]
	s_cbranch_vccnz .LBB0_1917
	ds_read2st64_b32 v[172:173], v200 offset1:2
	ds_read2st64_b32 v[174:175], v201 offset1:2
	v_mov_b32_e32 v177, v171
	s_waitcnt lgkmcnt(0)
	v_add_u32_e32 v172, v172, v1
	v_add_u32_e32 v170, v173, v1
	v_add_u32_e32 v174, v174, v1
	v_add_u32_e32 v176, v175, v1
	s_branch .LBB0_1917

; #define PG8_ROWS(_u) do { _Pragma("unroll") for (int _i = 0; _i < 2; ++_i) { voffA[_i] = S.row_off((_u), rselA[_i]) + cselA[_i]; voffA1[_i] = S.row_off((_u), HALF + rselA[_i]) + cselA[_i]; } } while (0)
; #define PG8_STAGE(bufoff, gbase, voff) do { _Pragma("unroll") for (int _i = 0; _i < 2; ++_i) \
;         __builtin_amdgcn_global_load_lds((const unsigned*)((const char*)(gbase) + (voff)[_i]), (PG8_LAS unsigned*)(lds + (bufoff) + ldsw + _i * 8192), 16, 0, 0); } while (0)
; #define PG8_WAIT_V(n) asm volatile("s_waitcnt vmcnt(" #n ")" ::: "memory")
; #define PG8_WAIT_L(n) asm volatile("s_waitcnt lgkmcnt(" #n ")" ::: "memory")
; #define PG8_BAR __builtin_amdgcn_s_barrier()
; #define PG8_SCHED __builtin_amdgcn_sched_barrier(0)
; template <class Epi, class Sched, bool ALIGN_EPI = false, bool SP2 = false, bool FP8 = false, bool I8 = false>
; __device__ __forceinline__ void gemm_phase(PG8_LAS unsigned char* lds, const Gemm g, const Sched& S, const Epi& E) {
;     ...
;             PG8_LDB(B0, 0, 0); PG8_LDB(B1, 0, 1); PG8_SCHED; PG8_LDA(At, 0, 0); PG8_STAGE(PG8_SA(1, 1), a1 + hstepA, voffA1);
;             PG8_WAIT_V(8); PG8_WAIT_L(0); PG8_BAR; PG8_MMA(0, 0, At, B0); PG8_MMA(0, 1, At, B1); PG8_BAR; PG8_SCHED;
;             if constexpr (Sched::GATHER) { if (last && has_next) PG8_ROWS(ui + 1); }
;             PG8_LDA(At, 0, 1); PG8_STAGE(PG8_SB(0, 0), b2, voffB); PG8_STAGE(PG8_SB(0, 1), b2 + hstep, voffB); PG8_STAGE(PG8_SA(0, 0), a2, voffA);
;             PG8_WAIT_V(8); PG8_WAIT_L(0); PG8_BAR; PG8_MMA(1, 0, At, B0); PG8_MMA(1, 1, At, B1); PG8_BAR; PG8_SCHED;
.LBB0_2397:
	ds_read_b128 v[16:19], v189
	ds_read_b128 v[20:23], v189 offset:1024
	ds_read_b128 v[24:27], v189 offset:2048
	ds_read_b128 v[28:31], v189 offset:3072
	ds_read_b128 v[0:3], v190
	ds_read_b128 v[4:7], v190 offset:1024
	ds_read_b128 v[8:11], v190 offset:2048
	ds_read_b128 v[12:15], v190 offset:3072
	s_add_u32 s28, s6, 0xfffc0080
	s_addc_u32 s29, s7, -1
	s_cmp_eq_u32 s52, 12
	s_cselect_b32 s31, s17, s29
	s_cselect_b32 s30, s19, s28
	s_cselect_b32 s29, s21, s51
	s_cselect_b32 s28, s20, s50
	v_lshl_add_u64 v[218:219], s[6:7], 0, v[172:173]
	s_add_i32 m0, s25, 0xc000
	ds_read_b128 v[176:179], v191
	ds_read_b128 v[180:183], v191 offset:1024
	ds_read_b128 v[194:197], v191 offset:2048
	ds_read_b128 v[198:201], v191 offset:3072
	ds_read_b128 v[202:205], v191 offset:4096
	ds_read_b128 v[206:209], v191 offset:5120
	ds_read_b128 v[210:213], v191 offset:6144
	ds_read_b128 v[214:217], v191 offset:7168
	global_load_lds_dwordx4 v[218:219], off
	v_lshl_add_u64 v[218:219], s[6:7], 0, v[174:175]
	s_add_i32 m0, s25, 0xe000
	s_nop 0
	global_load_lds_dwordx4 v[218:219], off
	s_waitcnt vmcnt(8)
	s_waitcnt lgkmcnt(0)
	s_barrier
	s_setprio 1
	s_waitcnt lgkmcnt(0)
	v_mfma_scale_f32_16x16x128_f8f6f4 v[156:159], v[16:23], v[176:183], v[156:159], v192, v192 op_sel_hi:[0,0,0]
	v_mfma_scale_f32_16x16x128_f8f6f4 v[152:155], v[24:31], v[176:183], v[152:155], v192, v192 op_sel_hi:[0,0,0]
	v_mfma_scale_f32_16x16x128_f8f6f4 v[148:151], v[16:23], v[194:201], v[148:151], v192, v192 op_sel_hi:[0,0,0]
	v_mfma_scale_f32_16x16x128_f8f6f4 v[144:147], v[24:31], v[194:201], v[144:147], v192, v192 op_sel_hi:[0,0,0]
	v_mfma_scale_f32_16x16x128_f8f6f4 v[140:143], v[16:23], v[202:209], v[140:143], v192, v192 op_sel_hi:[0,0,0]
	v_mfma_scale_f32_16x16x128_f8f6f4 v[136:139], v[24:31], v[202:209], v[136:139], v192, v192 op_sel_hi:[0,0,0]
	v_mfma_scale_f32_16x16x128_f8f6f4 v[132:135], v[16:23], v[210:217], v[132:135], v192, v192 op_sel_hi:[0,0,0]
	v_mfma_scale_f32_16x16x128_f8f6f4 v[128:131], v[24:31], v[210:217], v[128:131], v192, v192 op_sel_hi:[0,0,0]
	v_mfma_scale_f32_16x16x128_f8f6f4 v[104:107], v[0:7], v[176:183], v[104:107], v192, v192 op_sel_hi:[0,0,0]
	v_mfma_scale_f32_16x16x128_f8f6f4 v[92:95], v[8:15], v[176:183], v[92:95], v192, v192 op_sel_hi:[0,0,0]
	v_mfma_scale_f32_16x16x128_f8f6f4 v[88:91], v[0:7], v[194:201], v[88:91], v192, v192 op_sel_hi:[0,0,0]
	v_mfma_scale_f32_16x16x128_f8f6f4 v[80:83], v[8:15], v[194:201], v[80:83], v192, v192 op_sel_hi:[0,0,0]
	v_mfma_scale_f32_16x16x128_f8f6f4 v[76:79], v[0:7], v[202:209], v[76:79], v192, v192 op_sel_hi:[0,0,0]
	v_mfma_scale_f32_16x16x128_f8f6f4 v[72:75], v[8:15], v[202:209], v[72:75], v192, v192 op_sel_hi:[0,0,0]
	v_mfma_scale_f32_16x16x128_f8f6f4 v[68:71], v[0:7], v[210:217], v[68:71], v192, v192 op_sel_hi:[0,0,0]
	v_mfma_scale_f32_16x16x128_f8f6f4 v[64:67], v[8:15], v[210:217], v[64:67], v192, v192 op_sel_hi:[0,0,0]
	s_setprio 0
	s_barrier
	s_add_i32 s53, s43, s35
	v_lshl_add_u64 v[176:177], s[28:29], 0, v[168:169]
	s_mov_b32 m0, s53
	ds_read_b128 v[194:197], v191 offset:16384
	ds_read_b128 v[198:201], v191 offset:17408
	ds_read_b128 v[202:205], v191 offset:18432
	ds_read_b128 v[206:209], v191 offset:19456
	ds_read_b128 v[210:213], v191 offset:20480
	ds_read_b128 v[214:217], v191 offset:21504
	ds_read_b128 v[218:221], v191 offset:22528
	ds_read_b128 v[222:225], v191 offset:23552
	global_load_lds_dwordx4 v[176:177], off
	s_add_i32 m0, s53, 0x2000
	s_add_u32 s54, s28, 0x40000
	v_lshl_add_u64 v[178:179], s[28:29], 0, v[164:165]
	s_addc_u32 s55, s29, 0
	s_add_i32 s53, s44, s35
	global_load_lds_dwordx4 v[178:179], off
	v_lshl_add_u64 v[180:181], s[54:55], 0, v[168:169]
	s_mov_b32 m0, s53
	v_lshl_add_u64 v[182:183], s[30:31], 0, v[166:167]
	global_load_lds_dwordx4 v[180:181], off
	v_lshl_add_u64 v[180:181], s[54:55], 0, v[164:165]
	s_add_i32 m0, s53, 0x2000
	s_nop 0
	global_load_lds_dwordx4 v[180:181], off
	v_lshl_add_u64 v[180:181], s[30:31], 0, v[170:171]
	s_mov_b32 m0, s25
	s_nop 0
	global_load_lds_dwordx4 v[180:181], off
	s_mov_b32 m0, s27
	s_nop 0
	global_load_lds_dwordx4 v[182:183], off
	s_waitcnt vmcnt(8)
	s_waitcnt lgkmcnt(0)
	s_barrier
	s_setprio 1
	s_waitcnt lgkmcnt(0)
	v_mfma_scale_f32_16x16x128_f8f6f4 v[124:127], v[16:23], v[194:201], v[124:127], v192, v192 op_sel_hi:[0,0,0]
	v_mfma_scale_f32_16x16x128_f8f6f4 v[120:123], v[24:31], v[194:201], v[120:123], v192, v192 op_sel_hi:[0,0,0]
	v_mfma_scale_f32_16x16x128_f8f6f4 v[116:119], v[16:23], v[202:209], v[116:119], v192, v192 op_sel_hi:[0,0,0]
	v_mfma_scale_f32_16x16x128_f8f6f4 v[112:115], v[24:31], v[202:209], v[112:115], v192, v192 op_sel_hi:[0,0,0]
	v_mfma_scale_f32_16x16x128_f8f6f4 v[108:111], v[16:23], v[210:217], v[108:111], v192, v192 op_sel_hi:[0,0,0]
	v_mfma_scale_f32_16x16x128_f8f6f4 v[100:103], v[24:31], v[210:217], v[100:103], v192, v192 op_sel_hi:[0,0,0]
	v_mfma_scale_f32_16x16x128_f8f6f4 v[96:99], v[16:23], v[218:225], v[96:99], v192, v192 op_sel_hi:[0,0,0]
	v_mfma_scale_f32_16x16x128_f8f6f4 v[84:87], v[24:31], v[218:225], v[84:87], v192, v192 op_sel_hi:[0,0,0]
	v_mfma_scale_f32_16x16x128_f8f6f4 v[60:63], v[0:7], v[194:201], v[60:63], v192, v192 op_sel_hi:[0,0,0]
	v_mfma_scale_f32_16x16x128_f8f6f4 v[56:59], v[8:15], v[194:201], v[56:59], v192, v192 op_sel_hi:[0,0,0]
	v_mfma_scale_f32_16x16x128_f8f6f4 v[52:55], v[0:7], v[202:209], v[52:55], v192, v192 op_sel_hi:[0,0,0]
	v_mfma_scale_f32_16x16x128_f8f6f4 v[48:51], v[8:15], v[202:209], v[48:51], v192, v192 op_sel_hi:[0,0,0]
	v_mfma_scale_f32_16x16x128_f8f6f4 v[44:47], v[0:7], v[210:217], v[44:47], v192, v192 op_sel_hi:[0,0,0]
	v_mfma_scale_f32_16x16x128_f8f6f4 v[40:43], v[8:15], v[210:217], v[40:43], v192, v192 op_sel_hi:[0,0,0]
	v_mfma_scale_f32_16x16x128_f8f6f4 v[36:39], v[0:7], v[218:225], v[36:39], v192, v192 op_sel_hi:[0,0,0]
	v_mfma_scale_f32_16x16x128_f8f6f4 v[32:35], v[8:15], v[218:225], v[32:35], v192, v192 op_sel_hi:[0,0,0]
	s_setprio 0
	s_barrier
; #define PG8_STAGE(bufoff, gbase, voff) do { _Pragma("unroll") for (int _i = 0; _i < 2; ++_i) \
;         __builtin_amdgcn_global_load_lds((const unsigned*)((const char*)(gbase) + (voff)[_i]), (PG8_LAS unsigned*)(lds + (bufoff) + ldsw + _i * 8192), 16, 0, 0); } while (0)
; #define PG8_WAIT_V(n) asm volatile("s_waitcnt vmcnt(" #n ")" ::: "memory")
; #define PG8_WAIT_L(n) asm volatile("s_waitcnt lgkmcnt(" #n ")" ::: "memory")
; #define PG8_BAR __builtin_amdgcn_s_barrier()
; #define PG8_SCHED __builtin_amdgcn_sched_barrier(0)
; template <class Epi, class Sched, bool ALIGN_EPI = false, bool SP2 = false, bool FP8 = false, bool I8 = false>
; __device__ __forceinline__ void gemm_phase(PG8_LAS unsigned char* lds, const Gemm g, const Sched& S, const Epi& E) {
;     ...
;             PG8_LDB(B0, 1, 0); PG8_LDB(B1, 1, 1); PG8_SCHED; PG8_LDA(At, 1, 0); PG8_STAGE(PG8_SA(0, 1), a2 + hstepA, voffA1);
;             PG8_WAIT_V(8); PG8_WAIT_L(0); PG8_BAR; PG8_MMA(0, 0, At, B0); PG8_MMA(0, 1, At, B1); PG8_BAR; PG8_SCHED;
;             PG8_LDA(At, 1, 1); PG8_STAGE(PG8_SB(1, 0), b3, voffB); PG8_STAGE(PG8_SB(1, 1), b3 + hstep, voffB); PG8_STAGE(PG8_SA(1, 0), a3, voffA);
;             PG8_WAIT_V(8); PG8_WAIT_L(0); PG8_BAR; PG8_MMA(1, 0, At, B0); PG8_MMA(1, 1, At, B1); PG8_BAR; PG8_SCHED;
	s_add_i32 s53, 0, 0x18000
	s_add_i32 s54, 0, 0x1c000
	v_add_u32_e32 v12, s53, v163
	v_add_u32_e32 v28, s54, v163
	ds_read_b128 v[0:3], v12
	ds_read_b128 v[4:7], v12 offset:1024
	ds_read_b128 v[8:11], v12 offset:2048
	ds_read_b128 v[12:15], v12 offset:3072
	ds_read_b128 v[16:19], v28
	ds_read_b128 v[20:23], v28 offset:1024
	ds_read_b128 v[24:27], v28 offset:2048
	ds_read_b128 v[28:31], v28 offset:3072
	s_add_u32 s30, s30, 0x40000
	s_addc_u32 s31, s31, 0
	s_mov_b32 m0, s39
	v_lshl_add_u64 v[226:227], s[30:31], 0, v[170:171]
	ds_read_b128 v[194:197], v191 offset:32768
	ds_read_b128 v[198:201], v191 offset:33792
	ds_read_b128 v[202:205], v191 offset:34816
	ds_read_b128 v[206:209], v191 offset:35840
	ds_read_b128 v[210:213], v191 offset:36864
	ds_read_b128 v[214:217], v191 offset:37888
	ds_read_b128 v[218:221], v191 offset:38912
	ds_read_b128 v[222:225], v191 offset:39936
	global_load_lds_dwordx4 v[226:227], off
	v_lshl_add_u64 v[226:227], s[30:31], 0, v[166:167]
	s_mov_b32 m0, s40
	s_nop 0
	global_load_lds_dwordx4 v[226:227], off
	s_waitcnt vmcnt(8)
	s_waitcnt lgkmcnt(0)
	s_barrier
	s_setprio 1
	s_waitcnt lgkmcnt(0)
	v_mfma_scale_f32_16x16x128_f8f6f4 v[156:159], v[0:7], v[194:201], v[156:159], v192, v192 op_sel_hi:[0,0,0]
	v_mfma_scale_f32_16x16x128_f8f6f4 v[152:155], v[8:15], v[194:201], v[152:155], v192, v192 op_sel_hi:[0,0,0]
	v_mfma_scale_f32_16x16x128_f8f6f4 v[148:151], v[0:7], v[202:209], v[148:151], v192, v192 op_sel_hi:[0,0,0]
	v_mfma_scale_f32_16x16x128_f8f6f4 v[144:147], v[8:15], v[202:209], v[144:147], v192, v192 op_sel_hi:[0,0,0]
	v_mfma_scale_f32_16x16x128_f8f6f4 v[140:143], v[0:7], v[210:217], v[140:143], v192, v192 op_sel_hi:[0,0,0]
	v_mfma_scale_f32_16x16x128_f8f6f4 v[136:139], v[8:15], v[210:217], v[136:139], v192, v192 op_sel_hi:[0,0,0]
	v_mfma_scale_f32_16x16x128_f8f6f4 v[132:135], v[0:7], v[218:225], v[132:135], v192, v192 op_sel_hi:[0,0,0]
	v_mfma_scale_f32_16x16x128_f8f6f4 v[128:131], v[8:15], v[218:225], v[128:131], v192, v192 op_sel_hi:[0,0,0]
	v_mfma_scale_f32_16x16x128_f8f6f4 v[104:107], v[16:23], v[194:201], v[104:107], v192, v192 op_sel_hi:[0,0,0]
	v_mfma_scale_f32_16x16x128_f8f6f4 v[92:95], v[24:31], v[194:201], v[92:95], v192, v192 op_sel_hi:[0,0,0]
	v_mfma_scale_f32_16x16x128_f8f6f4 v[88:91], v[16:23], v[202:209], v[88:91], v192, v192 op_sel_hi:[0,0,0]
	v_mfma_scale_f32_16x16x128_f8f6f4 v[80:83], v[24:31], v[202:209], v[80:83], v192, v192 op_sel_hi:[0,0,0]
	v_mfma_scale_f32_16x16x128_f8f6f4 v[76:79], v[16:23], v[210:217], v[76:79], v192, v192 op_sel_hi:[0,0,0]
	v_mfma_scale_f32_16x16x128_f8f6f4 v[72:75], v[24:31], v[210:217], v[72:75], v192, v192 op_sel_hi:[0,0,0]
	v_mfma_scale_f32_16x16x128_f8f6f4 v[68:71], v[16:23], v[218:225], v[68:71], v192, v192 op_sel_hi:[0,0,0]
	v_mfma_scale_f32_16x16x128_f8f6f4 v[64:67], v[24:31], v[218:225], v[64:67], v192, v192 op_sel_hi:[0,0,0]
	s_setprio 0
	s_barrier
	s_add_i32 s30, s53, s35
	v_lshl_add_u64 v[176:177], v[176:177], 0, s[10:11]
	s_mov_b32 m0, s30
	ds_read_b128 v[194:197], v191 offset:49152
	ds_read_b128 v[198:201], v191 offset:50176
	ds_read_b128 v[202:205], v191 offset:51200
	ds_read_b128 v[206:209], v191 offset:52224
	ds_read_b128 v[210:213], v191 offset:53248
	ds_read_b128 v[214:217], v191 offset:54272
	ds_read_b128 v[218:221], v191 offset:55296
	ds_read_b128 v[222:225], v191 offset:56320
	global_load_lds_dwordx4 v[176:177], off
	s_add_i32 m0, s30, 0x2000
	s_add_u32 s28, s28, 0x40080
	v_lshl_add_u64 v[176:177], v[178:179], 0, s[10:11]
	s_addc_u32 s29, s29, 0
	s_add_i32 s30, s54, s35
	global_load_lds_dwordx4 v[176:177], off
	v_lshl_add_u64 v[176:177], s[28:29], 0, v[168:169]
	s_mov_b32 m0, s30
	s_nop 0
	global_load_lds_dwordx4 v[176:177], off
	v_lshl_add_u64 v[176:177], s[28:29], 0, v[164:165]
	s_add_i32 m0, s30, 0x2000
	s_nop 0
	global_load_lds_dwordx4 v[176:177], off
	v_lshl_add_u64 v[176:177], v[180:181], 0, s[10:11]
	s_mov_b32 m0, s41
	s_nop 0
	global_load_lds_dwordx4 v[176:177], off
	v_lshl_add_u64 v[176:177], v[182:183], 0, s[10:11]
	s_mov_b32 m0, s42
	s_nop 0
	global_load_lds_dwordx4 v[176:177], off
	s_waitcnt vmcnt(8)
	s_waitcnt lgkmcnt(0)
	s_barrier
	s_setprio 1
	s_waitcnt lgkmcnt(0)
	v_mfma_scale_f32_16x16x128_f8f6f4 v[124:127], v[0:7], v[194:201], v[124:127], v192, v192 op_sel_hi:[0,0,0]
	v_mfma_scale_f32_16x16x128_f8f6f4 v[120:123], v[8:15], v[194:201], v[120:123], v192, v192 op_sel_hi:[0,0,0]
	v_mfma_scale_f32_16x16x128_f8f6f4 v[116:119], v[0:7], v[202:209], v[116:119], v192, v192 op_sel_hi:[0,0,0]
	v_mfma_scale_f32_16x16x128_f8f6f4 v[112:115], v[8:15], v[202:209], v[112:115], v192, v192 op_sel_hi:[0,0,0]
	v_mfma_scale_f32_16x16x128_f8f6f4 v[108:111], v[0:7], v[210:217], v[108:111], v192, v192 op_sel_hi:[0,0,0]
	v_mfma_scale_f32_16x16x128_f8f6f4 v[100:103], v[8:15], v[210:217], v[100:103], v192, v192 op_sel_hi:[0,0,0]
	v_mfma_scale_f32_16x16x128_f8f6f4 v[96:99], v[0:7], v[218:225], v[96:99], v192, v192 op_sel_hi:[0,0,0]
	v_mfma_scale_f32_16x16x128_f8f6f4 v[84:87], v[8:15], v[218:225], v[84:87], v192, v192 op_sel_hi:[0,0,0]
	v_mfma_scale_f32_16x16x128_f8f6f4 v[60:63], v[16:23], v[194:201], v[60:63], v192, v192 op_sel_hi:[0,0,0]
	v_mfma_scale_f32_16x16x128_f8f6f4 v[56:59], v[24:31], v[194:201], v[56:59], v192, v192 op_sel_hi:[0,0,0]
	v_mfma_scale_f32_16x16x128_f8f6f4 v[52:55], v[16:23], v[202:209], v[52:55], v192, v192 op_sel_hi:[0,0,0]
	v_mfma_scale_f32_16x16x128_f8f6f4 v[48:51], v[24:31], v[202:209], v[48:51], v192, v192 op_sel_hi:[0,0,0]
	v_mfma_scale_f32_16x16x128_f8f6f4 v[44:47], v[16:23], v[210:217], v[44:47], v192, v192 op_sel_hi:[0,0,0]
	v_mfma_scale_f32_16x16x128_f8f6f4 v[40:43], v[24:31], v[210:217], v[40:43], v192, v192 op_sel_hi:[0,0,0]
	v_mfma_scale_f32_16x16x128_f8f6f4 v[36:39], v[16:23], v[218:225], v[36:39], v192, v192 op_sel_hi:[0,0,0]
	v_mfma_scale_f32_16x16x128_f8f6f4 v[32:35], v[24:31], v[218:225], v[32:35], v192, v192 op_sel_hi:[0,0,0]
	s_setprio 0
	s_barrier
	s_add_i32 s52, s52, 2
	s_add_u32 s6, s6, 0x100
	s_addc_u32 s7, s7, 0
	s_add_u32 s50, s50, 0x100
	s_addc_u32 s51, s51, 0
	s_cmp_gt_u32 s52, 13
	s_cbranch_scc0 .LBB0_2397
	s_and_b64 vcc, exec, s[12:13]
	s_cbranch_vccz .LBB0_2400
	s_barrier
